# P8 epilogue: 4x4 lane transposes (permlane32/16 swap) + 8 dwordx4 stores per wave instead of 32 dword stores
# speedup vs baseline: 1.0158x; 1.0128x over previous
.LBB0_1047:
	s_ashr_i32 s7, s6, 31
	s_lshl_b64 s[26:27], s[6:7], 13
	s_add_u32 s7, s86, s26
	s_addc_u32 s28, s87, s27
	s_ashr_i32 s11, s10, 31
	s_lshl_b64 s[26:27], s[10:11], 2
	s_add_u32 s7, s7, s26
	s_addc_u32 s27, s28, s27
	s_add_u32 s26, s7, s72
	s_addc_u32 s27, s27, 0
	global_load_dwordx4 v[12:15], v198, s[26:27]
	global_load_dwordx4 v[8:11], v198, s[26:27] offset:64
	global_load_dwordx4 v[4:7], v198, s[26:27] offset:512
	global_load_dwordx4 v[0:3], v198, s[26:27] offset:576
	s_andn2_b64 vcc, exec, s[24:25]
	v_bfe_u32 v251, v178, 4, 2
	v_lshl_add_u32 v16, v251, 4, v193
	v_add_u32_e32 v16, s44, v16
	s_mov_b64 s[100:101], 0x40000
	v_ashrrev_i32_e32 v17, 31, v16
	v_lshlrev_b64 v[252:253], 11, v[16:17]
	v_lshl_add_u64 v[252:253], s[16:17], 0, v[252:253]
	v_lshl_add_u64 v[252:253], v[252:253], 0, s[10:11]
	v_lshl_add_u64 v[252:253], v[252:253], 0, s[14:15]
	v_lshl_add_u64 v[254:255], v[252:253], 0, s[100:101]
	s_waitcnt vmcnt(0)
	v_pk_add_f32 v[24:25], v[172:173], v[12:13]
	v_pk_add_f32 v[26:27], v[174:175], v[14:15]
	v_pk_add_f32 v[28:29], v[164:165], v[12:13]
	v_pk_add_f32 v[30:31], v[166:167], v[14:15]
	v_pk_add_f32 v[32:33], v[156:157], v[12:13]
	v_pk_add_f32 v[34:35], v[158:159], v[14:15]
	v_pk_add_f32 v[36:37], v[148:149], v[12:13]
	v_pk_add_f32 v[38:39], v[150:151], v[14:15]
	v_med3_f32 v24, v24, s77, v200
	v_med3_f32 v25, v25, s77, v200
	v_med3_f32 v26, v26, s77, v200
	v_med3_f32 v27, v27, s77, v200
	v_med3_f32 v28, v28, s77, v200
	v_med3_f32 v29, v29, s77, v200
	v_med3_f32 v30, v30, s77, v200
	v_med3_f32 v31, v31, s77, v200
	v_med3_f32 v32, v32, s77, v200
	v_med3_f32 v33, v33, s77, v200
	v_med3_f32 v34, v34, s77, v200
	v_med3_f32 v35, v35, s77, v200
	v_med3_f32 v36, v36, s77, v200
	v_med3_f32 v37, v37, s77, v200
	v_med3_f32 v38, v38, s77, v200
	v_med3_f32 v39, v39, s77, v200
	v_cvt_pk_fp8_f32 v20, v24, v25
	v_cvt_pk_fp8_f32 v21, v28, v29
	v_cvt_pk_fp8_f32 v22, v32, v33
	v_cvt_pk_fp8_f32 v23, v36, v37
	v_cvt_pk_fp8_f32 v20, v26, v27 op_sel:[0,0,1]
	v_cvt_pk_fp8_f32 v21, v30, v31 op_sel:[0,0,1]
	v_cvt_pk_fp8_f32 v22, v34, v35 op_sel:[0,0,1]
	v_cvt_pk_fp8_f32 v23, v38, v39 op_sel:[0,0,1]
	s_nop 1
	v_permlane32_swap_b32_e32 v20, v22
	v_permlane32_swap_b32_e32 v21, v23
	s_nop 1
	v_permlane16_swap_b32_e32 v20, v21
	v_permlane16_swap_b32_e32 v22, v23
	global_store_dwordx4 v[252:253], v[20:23], off
	v_pk_add_f32 v[24:25], v[168:169], v[8:9]
	v_pk_add_f32 v[26:27], v[170:171], v[10:11]
	v_pk_add_f32 v[28:29], v[160:161], v[8:9]
	v_pk_add_f32 v[30:31], v[162:163], v[10:11]
	v_pk_add_f32 v[32:33], v[152:153], v[8:9]
	v_pk_add_f32 v[34:35], v[154:155], v[10:11]
	v_pk_add_f32 v[36:37], v[144:145], v[8:9]
	v_pk_add_f32 v[38:39], v[146:147], v[10:11]
	v_med3_f32 v24, v24, s77, v200
	v_med3_f32 v25, v25, s77, v200
	v_med3_f32 v26, v26, s77, v200
	v_med3_f32 v27, v27, s77, v200
	v_med3_f32 v28, v28, s77, v200
	v_med3_f32 v29, v29, s77, v200
	v_med3_f32 v30, v30, s77, v200
	v_med3_f32 v31, v31, s77, v200
	v_med3_f32 v32, v32, s77, v200
	v_med3_f32 v33, v33, s77, v200
	v_med3_f32 v34, v34, s77, v200
	v_med3_f32 v35, v35, s77, v200
	v_med3_f32 v36, v36, s77, v200
	v_med3_f32 v37, v37, s77, v200
	v_med3_f32 v38, v38, s77, v200
	v_med3_f32 v39, v39, s77, v200
	v_cvt_pk_fp8_f32 v40, v24, v25
	v_cvt_pk_fp8_f32 v41, v28, v29
	v_cvt_pk_fp8_f32 v42, v32, v33
	v_cvt_pk_fp8_f32 v43, v36, v37
	v_cvt_pk_fp8_f32 v40, v26, v27 op_sel:[0,0,1]
	v_cvt_pk_fp8_f32 v41, v30, v31 op_sel:[0,0,1]
	v_cvt_pk_fp8_f32 v42, v34, v35 op_sel:[0,0,1]
	v_cvt_pk_fp8_f32 v43, v38, v39 op_sel:[0,0,1]
	s_nop 1
	v_permlane32_swap_b32_e32 v40, v42
	v_permlane32_swap_b32_e32 v41, v43
	s_nop 1
	v_permlane16_swap_b32_e32 v40, v41
	v_permlane16_swap_b32_e32 v42, v43
	global_store_dwordx4 v[252:253], v[40:43], off offset:16
	v_pk_add_f32 v[24:25], v[140:141], v[4:5]
	v_pk_add_f32 v[26:27], v[142:143], v[6:7]
	v_pk_add_f32 v[28:29], v[132:133], v[4:5]
	v_pk_add_f32 v[30:31], v[134:135], v[6:7]
	v_pk_add_f32 v[32:33], v[124:125], v[4:5]
	v_pk_add_f32 v[34:35], v[126:127], v[6:7]
	v_pk_add_f32 v[36:37], v[116:117], v[4:5]
	v_pk_add_f32 v[38:39], v[118:119], v[6:7]
	v_med3_f32 v24, v24, s77, v200
	v_med3_f32 v25, v25, s77, v200
	v_med3_f32 v26, v26, s77, v200
	v_med3_f32 v27, v27, s77, v200
	v_med3_f32 v28, v28, s77, v200
	v_med3_f32 v29, v29, s77, v200
	v_med3_f32 v30, v30, s77, v200
	v_med3_f32 v31, v31, s77, v200
	v_med3_f32 v32, v32, s77, v200
	v_med3_f32 v33, v33, s77, v200
	v_med3_f32 v34, v34, s77, v200
	v_med3_f32 v35, v35, s77, v200
	v_med3_f32 v36, v36, s77, v200
	v_med3_f32 v37, v37, s77, v200
	v_med3_f32 v38, v38, s77, v200
	v_med3_f32 v39, v39, s77, v200
	v_cvt_pk_fp8_f32 v20, v24, v25
	v_cvt_pk_fp8_f32 v21, v28, v29
	v_cvt_pk_fp8_f32 v22, v32, v33
	v_cvt_pk_fp8_f32 v23, v36, v37
	v_cvt_pk_fp8_f32 v20, v26, v27 op_sel:[0,0,1]
	v_cvt_pk_fp8_f32 v21, v30, v31 op_sel:[0,0,1]
	v_cvt_pk_fp8_f32 v22, v34, v35 op_sel:[0,0,1]
	v_cvt_pk_fp8_f32 v23, v38, v39 op_sel:[0,0,1]
	s_nop 1
	v_permlane32_swap_b32_e32 v20, v22
	v_permlane32_swap_b32_e32 v21, v23
	s_nop 1
	v_permlane16_swap_b32_e32 v20, v21
	v_permlane16_swap_b32_e32 v22, v23
	global_store_dwordx4 v[252:253], v[20:23], off offset:128
	v_pk_add_f32 v[24:25], v[136:137], v[0:1]
	v_pk_add_f32 v[26:27], v[138:139], v[2:3]
	v_pk_add_f32 v[28:29], v[128:129], v[0:1]
	v_pk_add_f32 v[30:31], v[130:131], v[2:3]
	v_pk_add_f32 v[32:33], v[120:121], v[0:1]
	v_pk_add_f32 v[34:35], v[122:123], v[2:3]
	v_pk_add_f32 v[36:37], v[112:113], v[0:1]
	v_pk_add_f32 v[38:39], v[114:115], v[2:3]
	v_med3_f32 v24, v24, s77, v200
	v_med3_f32 v25, v25, s77, v200
	v_med3_f32 v26, v26, s77, v200
	v_med3_f32 v27, v27, s77, v200
	v_med3_f32 v28, v28, s77, v200
	v_med3_f32 v29, v29, s77, v200
	v_med3_f32 v30, v30, s77, v200
	v_med3_f32 v31, v31, s77, v200
	v_med3_f32 v32, v32, s77, v200
	v_med3_f32 v33, v33, s77, v200
	v_med3_f32 v34, v34, s77, v200
	v_med3_f32 v35, v35, s77, v200
	v_med3_f32 v36, v36, s77, v200
	v_med3_f32 v37, v37, s77, v200
	v_med3_f32 v38, v38, s77, v200
	v_med3_f32 v39, v39, s77, v200
	v_cvt_pk_fp8_f32 v40, v24, v25
	v_cvt_pk_fp8_f32 v41, v28, v29
	v_cvt_pk_fp8_f32 v42, v32, v33
	v_cvt_pk_fp8_f32 v43, v36, v37
	v_cvt_pk_fp8_f32 v40, v26, v27 op_sel:[0,0,1]
	v_cvt_pk_fp8_f32 v41, v30, v31 op_sel:[0,0,1]
	v_cvt_pk_fp8_f32 v42, v34, v35 op_sel:[0,0,1]
	v_cvt_pk_fp8_f32 v43, v38, v39 op_sel:[0,0,1]
	s_nop 1
	v_permlane32_swap_b32_e32 v40, v42
	v_permlane32_swap_b32_e32 v41, v43
	s_nop 1
	v_permlane16_swap_b32_e32 v40, v41
	v_permlane16_swap_b32_e32 v42, v43
	global_store_dwordx4 v[252:253], v[40:43], off offset:144
	v_pk_add_f32 v[24:25], v[108:109], v[12:13]
	v_pk_add_f32 v[26:27], v[110:111], v[14:15]
	v_pk_add_f32 v[28:29], v[100:101], v[12:13]
	v_pk_add_f32 v[30:31], v[102:103], v[14:15]
	v_pk_add_f32 v[32:33], v[92:93], v[12:13]
	v_pk_add_f32 v[34:35], v[94:95], v[14:15]
	v_pk_add_f32 v[36:37], v[84:85], v[12:13]
	v_pk_add_f32 v[38:39], v[86:87], v[14:15]
	v_med3_f32 v24, v24, s77, v200
	v_med3_f32 v25, v25, s77, v200
	v_med3_f32 v26, v26, s77, v200
	v_med3_f32 v27, v27, s77, v200
	v_med3_f32 v28, v28, s77, v200
	v_med3_f32 v29, v29, s77, v200
	v_med3_f32 v30, v30, s77, v200
	v_med3_f32 v31, v31, s77, v200
	v_med3_f32 v32, v32, s77, v200
	v_med3_f32 v33, v33, s77, v200
	v_med3_f32 v34, v34, s77, v200
	v_med3_f32 v35, v35, s77, v200
	v_med3_f32 v36, v36, s77, v200
	v_med3_f32 v37, v37, s77, v200
	v_med3_f32 v38, v38, s77, v200
	v_med3_f32 v39, v39, s77, v200
	v_cvt_pk_fp8_f32 v20, v24, v25
	v_cvt_pk_fp8_f32 v21, v28, v29
	v_cvt_pk_fp8_f32 v22, v32, v33
	v_cvt_pk_fp8_f32 v23, v36, v37
	v_cvt_pk_fp8_f32 v20, v26, v27 op_sel:[0,0,1]
	v_cvt_pk_fp8_f32 v21, v30, v31 op_sel:[0,0,1]
	v_cvt_pk_fp8_f32 v22, v34, v35 op_sel:[0,0,1]
	v_cvt_pk_fp8_f32 v23, v38, v39 op_sel:[0,0,1]
	s_nop 1
	v_permlane32_swap_b32_e32 v20, v22
	v_permlane32_swap_b32_e32 v21, v23
	s_nop 1
	v_permlane16_swap_b32_e32 v20, v21
	v_permlane16_swap_b32_e32 v22, v23
	global_store_dwordx4 v[254:255], v[20:23], off
	v_pk_add_f32 v[24:25], v[104:105], v[8:9]
	v_pk_add_f32 v[26:27], v[106:107], v[10:11]
	v_pk_add_f32 v[28:29], v[96:97], v[8:9]
	v_pk_add_f32 v[30:31], v[98:99], v[10:11]
	v_pk_add_f32 v[32:33], v[88:89], v[8:9]
	v_pk_add_f32 v[34:35], v[90:91], v[10:11]
	v_pk_add_f32 v[36:37], v[80:81], v[8:9]
	v_pk_add_f32 v[38:39], v[82:83], v[10:11]
	v_med3_f32 v24, v24, s77, v200
	v_med3_f32 v25, v25, s77, v200
	v_med3_f32 v26, v26, s77, v200
	v_med3_f32 v27, v27, s77, v200
	v_med3_f32 v28, v28, s77, v200
	v_med3_f32 v29, v29, s77, v200
	v_med3_f32 v30, v30, s77, v200
	v_med3_f32 v31, v31, s77, v200
	v_med3_f32 v32, v32, s77, v200
	v_med3_f32 v33, v33, s77, v200
	v_med3_f32 v34, v34, s77, v200
	v_med3_f32 v35, v35, s77, v200
	v_med3_f32 v36, v36, s77, v200
	v_med3_f32 v37, v37, s77, v200
	v_med3_f32 v38, v38, s77, v200
	v_med3_f32 v39, v39, s77, v200
	v_cvt_pk_fp8_f32 v40, v24, v25
	v_cvt_pk_fp8_f32 v41, v28, v29
	v_cvt_pk_fp8_f32 v42, v32, v33
	v_cvt_pk_fp8_f32 v43, v36, v37
	v_cvt_pk_fp8_f32 v40, v26, v27 op_sel:[0,0,1]
	v_cvt_pk_fp8_f32 v41, v30, v31 op_sel:[0,0,1]
	v_cvt_pk_fp8_f32 v42, v34, v35 op_sel:[0,0,1]
	v_cvt_pk_fp8_f32 v43, v38, v39 op_sel:[0,0,1]
	s_nop 1
	v_permlane32_swap_b32_e32 v40, v42
	v_permlane32_swap_b32_e32 v41, v43
	s_nop 1
	v_permlane16_swap_b32_e32 v40, v41
	v_permlane16_swap_b32_e32 v42, v43
	global_store_dwordx4 v[254:255], v[40:43], off offset:16
	v_pk_add_f32 v[24:25], v[76:77], v[4:5]
	v_pk_add_f32 v[26:27], v[78:79], v[6:7]
	v_pk_add_f32 v[28:29], v[68:69], v[4:5]
	v_pk_add_f32 v[30:31], v[70:71], v[6:7]
	v_pk_add_f32 v[32:33], v[60:61], v[4:5]
	v_pk_add_f32 v[34:35], v[62:63], v[6:7]
	v_pk_add_f32 v[36:37], v[52:53], v[4:5]
	v_pk_add_f32 v[38:39], v[54:55], v[6:7]
	v_med3_f32 v24, v24, s77, v200
	v_med3_f32 v25, v25, s77, v200
	v_med3_f32 v26, v26, s77, v200
	v_med3_f32 v27, v27, s77, v200
	v_med3_f32 v28, v28, s77, v200
	v_med3_f32 v29, v29, s77, v200
	v_med3_f32 v30, v30, s77, v200
	v_med3_f32 v31, v31, s77, v200
	v_med3_f32 v32, v32, s77, v200
	v_med3_f32 v33, v33, s77, v200
	v_med3_f32 v34, v34, s77, v200
	v_med3_f32 v35, v35, s77, v200
	v_med3_f32 v36, v36, s77, v200
	v_med3_f32 v37, v37, s77, v200
	v_med3_f32 v38, v38, s77, v200
	v_med3_f32 v39, v39, s77, v200
	v_cvt_pk_fp8_f32 v20, v24, v25
	v_cvt_pk_fp8_f32 v21, v28, v29
	v_cvt_pk_fp8_f32 v22, v32, v33
	v_cvt_pk_fp8_f32 v23, v36, v37
	v_cvt_pk_fp8_f32 v20, v26, v27 op_sel:[0,0,1]
	v_cvt_pk_fp8_f32 v21, v30, v31 op_sel:[0,0,1]
	v_cvt_pk_fp8_f32 v22, v34, v35 op_sel:[0,0,1]
	v_cvt_pk_fp8_f32 v23, v38, v39 op_sel:[0,0,1]
	s_nop 1
	v_permlane32_swap_b32_e32 v20, v22
	v_permlane32_swap_b32_e32 v21, v23
	s_nop 1
	v_permlane16_swap_b32_e32 v20, v21
	v_permlane16_swap_b32_e32 v22, v23
	global_store_dwordx4 v[254:255], v[20:23], off offset:128
	v_pk_add_f32 v[24:25], v[72:73], v[0:1]
	v_pk_add_f32 v[26:27], v[74:75], v[2:3]
	v_pk_add_f32 v[28:29], v[64:65], v[0:1]
	v_pk_add_f32 v[30:31], v[66:67], v[2:3]
	v_pk_add_f32 v[32:33], v[56:57], v[0:1]
	v_pk_add_f32 v[34:35], v[58:59], v[2:3]
	v_pk_add_f32 v[36:37], v[48:49], v[0:1]
	v_pk_add_f32 v[38:39], v[50:51], v[2:3]
	v_med3_f32 v24, v24, s77, v200
	v_med3_f32 v25, v25, s77, v200
	v_med3_f32 v26, v26, s77, v200
	v_med3_f32 v27, v27, s77, v200
	v_med3_f32 v28, v28, s77, v200
	v_med3_f32 v29, v29, s77, v200
	v_med3_f32 v30, v30, s77, v200
	v_med3_f32 v31, v31, s77, v200
	v_med3_f32 v32, v32, s77, v200
	v_med3_f32 v33, v33, s77, v200
	v_med3_f32 v34, v34, s77, v200
	v_med3_f32 v35, v35, s77, v200
	v_med3_f32 v36, v36, s77, v200
	v_med3_f32 v37, v37, s77, v200
	v_med3_f32 v38, v38, s77, v200
	v_med3_f32 v39, v39, s77, v200
	v_cvt_pk_fp8_f32 v40, v24, v25
	v_cvt_pk_fp8_f32 v41, v28, v29
	v_cvt_pk_fp8_f32 v42, v32, v33
	v_cvt_pk_fp8_f32 v43, v36, v37
	v_cvt_pk_fp8_f32 v40, v26, v27 op_sel:[0,0,1]
	v_cvt_pk_fp8_f32 v41, v30, v31 op_sel:[0,0,1]
	v_cvt_pk_fp8_f32 v42, v34, v35 op_sel:[0,0,1]
	v_cvt_pk_fp8_f32 v43, v38, v39 op_sel:[0,0,1]
	s_nop 1
	v_permlane32_swap_b32_e32 v40, v42
	v_permlane32_swap_b32_e32 v41, v43
	s_nop 1
	v_permlane16_swap_b32_e32 v40, v41
	v_permlane16_swap_b32_e32 v42, v43
	global_store_dwordx4 v[254:255], v[40:43], off offset:144
	s_cbranch_vccnz .LBB0_994
	v_mov_b32_e32 v48, 0
	s_mov_b32 s81, s79
	s_mov_b64 s[8:9], s[22:23]
	s_mov_b32 s6, s20
	s_mov_b32 s44, s82
	s_mov_b32 s10, s21
	s_mov_b32 s80, s71
	v_mov_b32_e32 v49, v48
	v_mov_b32_e32 v50, v48
	v_mov_b32_e32 v51, v48
	v_mov_b32_e32 v52, v48
	v_mov_b32_e32 v53, v48
	v_mov_b32_e32 v54, v48
	v_mov_b32_e32 v55, v48
	v_mov_b32_e32 v56, v48
	v_mov_b32_e32 v57, v48
	v_mov_b32_e32 v58, v48
	v_mov_b32_e32 v59, v48
	v_mov_b32_e32 v60, v48
	v_mov_b32_e32 v61, v48
	v_mov_b32_e32 v62, v48
	v_mov_b32_e32 v63, v48
	v_mov_b32_e32 v64, v48
	v_mov_b32_e32 v65, v48
	v_mov_b32_e32 v66, v48
	v_mov_b32_e32 v67, v48
	v_mov_b32_e32 v68, v48
	v_mov_b32_e32 v69, v48
	v_mov_b32_e32 v70, v48
	v_mov_b32_e32 v71, v48
	v_mov_b32_e32 v72, v48
	v_mov_b32_e32 v73, v48
	v_mov_b32_e32 v74, v48
	v_mov_b32_e32 v75, v48
	v_mov_b32_e32 v76, v48
	v_mov_b32_e32 v77, v48
	v_mov_b32_e32 v78, v48
	v_mov_b32_e32 v79, v48
	v_mov_b32_e32 v80, v48
	v_mov_b32_e32 v81, v48
	v_mov_b32_e32 v82, v48
	v_mov_b32_e32 v83, v48
	v_mov_b32_e32 v84, v48
	v_mov_b32_e32 v85, v48
	v_mov_b32_e32 v86, v48
	v_mov_b32_e32 v87, v48
	v_mov_b32_e32 v88, v48
	v_mov_b32_e32 v89, v48
	v_mov_b32_e32 v90, v48
	v_mov_b32_e32 v91, v48
	v_mov_b32_e32 v92, v48
	v_mov_b32_e32 v93, v48
	v_mov_b32_e32 v94, v48
	v_mov_b32_e32 v95, v48
	v_mov_b32_e32 v96, v48
	v_mov_b32_e32 v97, v48
	v_mov_b32_e32 v98, v48
	v_mov_b32_e32 v99, v48
	v_mov_b32_e32 v100, v48
	v_mov_b32_e32 v101, v48
	v_mov_b32_e32 v102, v48
	v_mov_b32_e32 v103, v48
	v_mov_b32_e32 v104, v48
	v_mov_b32_e32 v105, v48
	v_mov_b32_e32 v106, v48
	v_mov_b32_e32 v107, v48
	v_mov_b32_e32 v108, v48
	v_mov_b32_e32 v109, v48
	v_mov_b32_e32 v110, v48
	v_mov_b32_e32 v111, v48
	v_mov_b32_e32 v112, v48
	v_mov_b32_e32 v113, v48
	v_mov_b32_e32 v114, v48
	v_mov_b32_e32 v115, v48
	v_mov_b32_e32 v116, v48
	v_mov_b32_e32 v117, v48
	v_mov_b32_e32 v118, v48
	v_mov_b32_e32 v119, v48
	v_mov_b32_e32 v120, v48
	v_mov_b32_e32 v121, v48
	v_mov_b32_e32 v122, v48
	v_mov_b32_e32 v123, v48
	v_mov_b32_e32 v124, v48
	v_mov_b32_e32 v125, v48
	v_mov_b32_e32 v126, v48
	v_mov_b32_e32 v127, v48
	v_mov_b32_e32 v128, v48
	v_mov_b32_e32 v129, v48
	v_mov_b32_e32 v130, v48
	v_mov_b32_e32 v131, v48
	v_mov_b32_e32 v132, v48
	v_mov_b32_e32 v133, v48
	v_mov_b32_e32 v134, v48
	v_mov_b32_e32 v135, v48
	v_mov_b32_e32 v136, v48
	v_mov_b32_e32 v137, v48
	v_mov_b32_e32 v138, v48
	v_mov_b32_e32 v139, v48
	v_mov_b32_e32 v140, v48
	v_mov_b32_e32 v141, v48
	v_mov_b32_e32 v142, v48
	v_mov_b32_e32 v143, v48
	v_mov_b32_e32 v144, v48
	v_mov_b32_e32 v145, v48
	v_mov_b32_e32 v146, v48
	v_mov_b32_e32 v147, v48
	v_mov_b32_e32 v148, v48
	v_mov_b32_e32 v149, v48
	v_mov_b32_e32 v150, v48
	v_mov_b32_e32 v151, v48
	v_mov_b32_e32 v152, v48
	v_mov_b32_e32 v153, v48
	v_mov_b32_e32 v154, v48
	v_mov_b32_e32 v155, v48
	v_mov_b32_e32 v156, v48
	v_mov_b32_e32 v157, v48
	v_mov_b32_e32 v158, v48
	v_mov_b32_e32 v159, v48
	v_mov_b32_e32 v160, v48
	v_mov_b32_e32 v161, v48
	v_mov_b32_e32 v162, v48
	v_mov_b32_e32 v163, v48
	v_mov_b32_e32 v164, v48
	v_mov_b32_e32 v165, v48
	v_mov_b32_e32 v166, v48
	v_mov_b32_e32 v167, v48
	v_mov_b32_e32 v168, v48
	v_mov_b32_e32 v169, v48
	v_mov_b32_e32 v170, v48
	v_mov_b32_e32 v171, v48
	v_mov_b32_e32 v172, v48
	v_mov_b32_e32 v173, v48
	v_mov_b32_e32 v174, v48
	v_mov_b32_e32 v175, v48
	s_branch .LBB0_994

	.amdhsa_kernel _Z4mega8MegaArgs
		.amdhsa_group_segment_fixed_size 256
		.amdhsa_private_segment_fixed_size 0
		.amdhsa_kernarg_size 424
		.amdhsa_user_sgpr_count 2
		.amdhsa_user_sgpr_dispatch_ptr 0
		.amdhsa_user_sgpr_queue_ptr 0
		.amdhsa_user_sgpr_kernarg_segment_ptr 1
		.amdhsa_user_sgpr_dispatch_id 0
		.amdhsa_user_sgpr_kernarg_preload_length 0
		.amdhsa_user_sgpr_kernarg_preload_offset 0
		.amdhsa_user_sgpr_private_segment_size 0
		.amdhsa_uses_dynamic_stack 0
		.amdhsa_enable_private_segment 0
		.amdhsa_system_sgpr_workgroup_id_x 1
		.amdhsa_system_sgpr_workgroup_id_y 0
		.amdhsa_system_sgpr_workgroup_id_z 0
		.amdhsa_system_sgpr_workgroup_info 0
		.amdhsa_system_vgpr_workitem_id 2
		.amdhsa_next_free_vgpr 256
		.amdhsa_next_free_sgpr 102
		.amdhsa_accum_offset 256
		.amdhsa_reserve_vcc 1
		.amdhsa_float_round_mode_32 0
		.amdhsa_float_round_mode_16_64 0
		.amdhsa_float_denorm_mode_32 3
		.amdhsa_float_denorm_mode_16_64 3
		.amdhsa_dx10_clamp 1
		.amdhsa_ieee_mode 1
		.amdhsa_fp16_overflow 0
		.amdhsa_tg_split 0
		.amdhsa_exception_fp_ieee_invalid_op 0
		.amdhsa_exception_fp_denorm_src 0
		.amdhsa_exception_fp_ieee_div_zero 0
		.amdhsa_exception_fp_ieee_overflow 0
		.amdhsa_exception_fp_ieee_underflow 0
		.amdhsa_exception_fp_ieee_inexact 0
		.amdhsa_exception_int_div_zero 0
	.end_amdhsa_kernel

amdhsa.kernels:
  - .agpr_count:     0
    .args:
      - .offset:         0
        .size:           168
        .value_kind:     by_value
      - .offset:         168
        .size:           4
        .value_kind:     hidden_block_count_x
      - .offset:         172
        .size:           4
        .value_kind:     hidden_block_count_y
      - .offset:         176
        .size:           4
        .value_kind:     hidden_block_count_z
      - .offset:         180
        .size:           2
        .value_kind:     hidden_group_size_x
      - .offset:         182
        .size:           2
        .value_kind:     hidden_group_size_y
      - .offset:         184
        .size:           2
        .value_kind:     hidden_group_size_z
      - .offset:         186
        .size:           2
        .value_kind:     hidden_remainder_x
      - .offset:         188
        .size:           2
        .value_kind:     hidden_remainder_y
      - .offset:         190
        .size:           2
        .value_kind:     hidden_remainder_z
      - .offset:         208
        .size:           8
        .value_kind:     hidden_global_offset_x
      - .offset:         216
        .size:           8
        .value_kind:     hidden_global_offset_y
      - .offset:         224
        .size:           8
        .value_kind:     hidden_global_offset_z
      - .offset:         232
        .size:           2
        .value_kind:     hidden_grid_dims
      - .offset:         288
        .size:           4
        .value_kind:     hidden_dynamic_lds_size
    .group_segment_fixed_size: 256
    .kernarg_segment_align: 8
    .kernarg_segment_size: 424
    .language:       OpenCL C
    .language_version:
      - 2
      - 0
    .max_flat_workgroup_size: 512
    .name:           _Z4mega8MegaArgs
    .private_segment_fixed_size: 0
    .sgpr_count:     108
    .sgpr_spill_count: 40
    .symbol:         _Z4mega8MegaArgs.kd
    .uniform_work_group_size: 1
    .uses_dynamic_stack: false
    .vgpr_count:     256
    .vgpr_spill_count: 0
    .wavefront_size: 64
